# waitcnt placement: first two QK tiles' bpermutes issued before the wait for the query fragment loads (vmcnt(2) covers the K gathers only)
# baseline (speedup 1.0000x reference)
.Lmy_dsa_fast:
	v_addc_co_u32_e32 v45, vcc, 0, v45, vcc
	global_load_dwordx4 v[44:47], v[44:45], off
	s_nop 0
	global_load_dwordx4 v[138:141], v[134:135], off offset:64
	s_waitcnt vmcnt(2)
	ds_bpermute_b32 v102, v248, v0
	ds_bpermute_b32 v103, v248, v1
	ds_bpermute_b32 v104, v248, v2
	ds_bpermute_b32 v105, v248, v3
	ds_bpermute_b32 v106, v248, v4
	ds_bpermute_b32 v107, v248, v5
	ds_bpermute_b32 v108, v248, v6
	ds_bpermute_b32 v109, v248, v7
	ds_bpermute_b32 v110, v248, v8
	ds_bpermute_b32 v111, v248, v9
	ds_bpermute_b32 v112, v248, v10
	ds_bpermute_b32 v113, v248, v11
	ds_bpermute_b32 v114, v248, v12
	ds_bpermute_b32 v115, v248, v13
	ds_bpermute_b32 v116, v248, v14
	ds_bpermute_b32 v117, v248, v15
	s_waitcnt vmcnt(1)
	v_cndmask_b32_e64 v137, v47, 0, s[38:39]
	v_cndmask_b32_e64 v136, v46, 0, s[38:39]
	v_cndmask_b32_e64 v135, v45, 0, s[38:39]
	v_cndmask_b32_e64 v134, v44, 0, s[38:39]
	s_waitcnt vmcnt(0)
	v_cndmask_b32_e64 v47, v141, 0, s[38:39]
	v_cndmask_b32_e64 v46, v140, 0, s[38:39]
	v_cndmask_b32_e64 v45, v139, 0, s[38:39]
	v_cndmask_b32_e64 v44, v138, 0, s[38:39]
	s_waitcnt lgkmcnt(12)
	v_mfma_f32_16x16x32_bf16 v[140:143], v[102:105], v[134:137], 0
	s_waitcnt lgkmcnt(8)
	v_mfma_f32_16x16x32_bf16 v[142:145], v[106:109], v[44:47], v[140:143]
	ds_bpermute_b32 v102, v248, v16
	ds_bpermute_b32 v103, v248, v17
	ds_bpermute_b32 v104, v248, v18
	ds_bpermute_b32 v105, v248, v19
	ds_bpermute_b32 v106, v248, v20
	ds_bpermute_b32 v107, v248, v21
	ds_bpermute_b32 v108, v248, v22
	ds_bpermute_b32 v109, v248, v23
	s_nop 1
	v_pk_mul_f32 v[142:143], v[142:143], s[74:75] op_sel_hi:[1,0]
	v_pk_mul_f32 v[140:141], v[144:145], s[74:75] op_sel_hi:[1,0]
	v_max3_f32 v49, v142, s82, v143
	v_max3_f32 v49, v49, v140, v141
	s_waitcnt lgkmcnt(12)
	v_mfma_f32_16x16x32_bf16 v[154:157], v[110:113], v[134:137], 0
	s_waitcnt lgkmcnt(8)
	v_mfma_f32_16x16x32_bf16 v[154:157], v[114:117], v[44:47], v[154:157]
	ds_bpermute_b32 v110, v248, v24
	ds_bpermute_b32 v111, v248, v25
	ds_bpermute_b32 v112, v248, v26
	ds_bpermute_b32 v113, v248, v27
	ds_bpermute_b32 v114, v248, v28
	ds_bpermute_b32 v115, v248, v29
	ds_bpermute_b32 v116, v248, v30
	ds_bpermute_b32 v117, v248, v31
	s_nop 1
	v_pk_mul_f32 v[144:145], v[154:155], s[74:75] op_sel_hi:[1,0]
	v_pk_mul_f32 v[138:139], v[156:157], s[74:75] op_sel_hi:[1,0]
	v_max3_f32 v49, v49, v144, v145
	v_max3_f32 v49, v49, v138, v139
	s_waitcnt lgkmcnt(12)
	v_mfma_f32_16x16x32_bf16 v[156:159], v[102:105], v[134:137], 0
	s_waitcnt lgkmcnt(8)
	v_mfma_f32_16x16x32_bf16 v[158:161], v[106:109], v[44:47], v[156:159]
	ds_bpermute_b32 v102, v248, v32
	ds_bpermute_b32 v103, v248, v33
	ds_bpermute_b32 v104, v248, v34
	ds_bpermute_b32 v105, v248, v35
	ds_bpermute_b32 v106, v248, v36
	ds_bpermute_b32 v107, v248, v37
	ds_bpermute_b32 v108, v248, v38
	ds_bpermute_b32 v109, v248, v39
	s_nop 1
	v_pk_mul_f32 v[158:159], v[158:159], s[74:75] op_sel_hi:[1,0]
	v_pk_mul_f32 v[156:157], v[160:161], s[74:75] op_sel_hi:[1,0]
	v_max3_f32 v49, v49, v158, v159
	v_max3_f32 v49, v49, v156, v157
	s_waitcnt lgkmcnt(12)
	v_mfma_f32_16x16x32_bf16 v[160:163], v[110:113], v[134:137], 0
	s_waitcnt lgkmcnt(8)
	v_mfma_f32_16x16x32_bf16 v[160:163], v[114:117], v[44:47], v[160:163]
	ds_bpermute_b32 v110, v248, v40
	ds_bpermute_b32 v111, v248, v41
	ds_bpermute_b32 v112, v248, v42
	ds_bpermute_b32 v113, v248, v43
	ds_bpermute_b32 v114, v248, v50
	ds_bpermute_b32 v115, v248, v51
	ds_bpermute_b32 v116, v248, v52
	ds_bpermute_b32 v117, v248, v53
	s_nop 1
	v_pk_mul_f32 v[160:161], v[160:161], s[74:75] op_sel_hi:[1,0]
	v_pk_mul_f32 v[154:155], v[162:163], s[74:75] op_sel_hi:[1,0]
	v_max3_f32 v49, v49, v160, v161
	v_max3_f32 v49, v49, v154, v155
	s_waitcnt lgkmcnt(12)
	v_mfma_f32_16x16x32_bf16 v[164:167], v[102:105], v[134:137], 0
	s_waitcnt lgkmcnt(8)
	v_mfma_f32_16x16x32_bf16 v[166:169], v[106:109], v[44:47], v[164:167]
	ds_bpermute_b32 v102, v248, v54
	ds_bpermute_b32 v103, v248, v55
	ds_bpermute_b32 v104, v248, v56
	ds_bpermute_b32 v105, v248, v57
	ds_bpermute_b32 v106, v248, v58
	ds_bpermute_b32 v107, v248, v59
	ds_bpermute_b32 v108, v248, v60
	ds_bpermute_b32 v109, v248, v61
	s_nop 1
	v_pk_mul_f32 v[166:167], v[166:167], s[74:75] op_sel_hi:[1,0]
	v_pk_mul_f32 v[164:165], v[168:169], s[74:75] op_sel_hi:[1,0]
	v_max3_f32 v49, v49, v166, v167
	v_max3_f32 v49, v49, v164, v165
	s_waitcnt lgkmcnt(12)
	v_mfma_f32_16x16x32_bf16 v[168:171], v[110:113], v[134:137], 0
	s_waitcnt lgkmcnt(8)
	v_mfma_f32_16x16x32_bf16 v[168:171], v[114:117], v[44:47], v[168:171]
	ds_bpermute_b32 v110, v248, v62
	ds_bpermute_b32 v111, v248, v63
	ds_bpermute_b32 v112, v248, v64
	ds_bpermute_b32 v113, v248, v65
	ds_bpermute_b32 v114, v248, v66
	ds_bpermute_b32 v115, v248, v67
	ds_bpermute_b32 v116, v248, v68
	ds_bpermute_b32 v117, v248, v69
	s_nop 1
	v_pk_mul_f32 v[168:169], v[168:169], s[74:75] op_sel_hi:[1,0]
	v_pk_mul_f32 v[162:163], v[170:171], s[74:75] op_sel_hi:[1,0]
	v_max3_f32 v49, v49, v168, v169
	v_max3_f32 v49, v49, v162, v163
	s_waitcnt lgkmcnt(12)
	v_mfma_f32_16x16x32_bf16 v[172:175], v[102:105], v[134:137], 0
	s_waitcnt lgkmcnt(8)
	v_mfma_f32_16x16x32_bf16 v[174:177], v[106:109], v[44:47], v[172:175]
	s_nop 7
	v_pk_mul_f32 v[174:175], v[174:175], s[74:75] op_sel_hi:[1,0]
	v_pk_mul_f32 v[172:173], v[176:177], s[74:75] op_sel_hi:[1,0]
	v_max3_f32 v49, v49, v174, v175
	v_max3_f32 v49, v49, v172, v173
	s_waitcnt lgkmcnt(4)
	v_mfma_f32_16x16x32_bf16 v[176:179], v[110:113], v[134:137], 0
	s_waitcnt lgkmcnt(0)
	v_mfma_f32_16x16x32_bf16 v[176:179], v[114:117], v[44:47], v[176:179]
	s_nop 7
	v_pk_mul_f32 v[176:177], v[176:177], s[74:75] op_sel_hi:[1,0]
	v_pk_mul_f32 v[170:171], v[178:179], s[74:75] op_sel_hi:[1,0]
	v_max3_f32 v49, v49, v176, v177
	v_max3_f32 v49, v49, v170, v171
	s_lshl_b32 s6, s6, 9
	s_add_i32 s19, s6, 0
	s_add_i32 s19, s19, 0x20000
	v_lshl_add_u32 v151, v147, 1, s19
	ds_read_u16 v0, v151 offset:256
	ds_read_u16 v8, v151 offset:288
	ds_read_u16 v16, v151 offset:320
	ds_read_u16 v24, v151 offset:352
	ds_read_u16 v32, v151 offset:384
	ds_read_u16 v40, v151 offset:416
	ds_read_u16 v54, v151 offset:448
	ds_read_u16 v62, v151 offset:480
	s_waitcnt lgkmcnt(0)
	v_lshl_or_b32 v4, v0, 8, v246
	global_load_dwordx4 v[0:3], v4, s[50:51]
	global_load_dwordx4 v[4:7], v4, s[50:51] offset:64
	v_lshl_or_b32 v12, v8, 8, v246
	global_load_dwordx4 v[8:11], v12, s[50:51]
	global_load_dwordx4 v[12:15], v12, s[50:51] offset:64
	v_lshl_or_b32 v20, v16, 8, v246
	global_load_dwordx4 v[16:19], v20, s[50:51]
	global_load_dwordx4 v[20:23], v20, s[50:51] offset:64
	v_lshl_or_b32 v28, v24, 8, v246
	global_load_dwordx4 v[24:27], v28, s[50:51]
	global_load_dwordx4 v[28:31], v28, s[50:51] offset:64
	v_lshl_or_b32 v36, v32, 8, v246
	global_load_dwordx4 v[32:35], v36, s[50:51]
	global_load_dwordx4 v[36:39], v36, s[50:51] offset:64
	v_lshl_or_b32 v50, v40, 8, v246
	global_load_dwordx4 v[40:43], v50, s[50:51]
	global_load_dwordx4 v[50:53], v50, s[50:51] offset:64
	v_lshl_or_b32 v58, v54, 8, v246
	global_load_dwordx4 v[54:57], v58, s[50:51]
	global_load_dwordx4 v[58:61], v58, s[50:51] offset:64
	v_lshl_or_b32 v66, v62, 8, v246
	global_load_dwordx4 v[62:65], v66, s[50:51]
	global_load_dwordx4 v[66:69], v66, s[50:51] offset:64
	s_xor_b64 s[6:7], s[44:45], -1
	s_ashr_i32 s53, s52, 31
	s_waitcnt vmcnt(15)
	ds_bpermute_b32 v102, v248, v0
	ds_bpermute_b32 v103, v248, v1
	ds_bpermute_b32 v104, v248, v2
	ds_bpermute_b32 v105, v248, v3
	s_waitcnt vmcnt(14)
	ds_bpermute_b32 v106, v248, v4
	ds_bpermute_b32 v107, v248, v5
	ds_bpermute_b32 v108, v248, v6
	ds_bpermute_b32 v109, v248, v7
	s_waitcnt vmcnt(13)
	ds_bpermute_b32 v110, v248, v8
	ds_bpermute_b32 v111, v248, v9
	ds_bpermute_b32 v112, v248, v10
	ds_bpermute_b32 v113, v248, v11
	s_waitcnt vmcnt(12)
	ds_bpermute_b32 v114, v248, v12
	ds_bpermute_b32 v115, v248, v13
	ds_bpermute_b32 v116, v248, v14
	ds_bpermute_b32 v117, v248, v15
	s_waitcnt lgkmcnt(12)
	v_mfma_f32_16x16x32_bf16 v[180:183], v[102:105], v[134:137], 0
	s_waitcnt lgkmcnt(8)
	v_mfma_f32_16x16x32_bf16 v[182:185], v[106:109], v[44:47], v[180:183]
	s_waitcnt vmcnt(11)
	ds_bpermute_b32 v102, v248, v16
	ds_bpermute_b32 v103, v248, v17
	ds_bpermute_b32 v104, v248, v18
	ds_bpermute_b32 v105, v248, v19
	s_waitcnt vmcnt(10)
	ds_bpermute_b32 v106, v248, v20
	ds_bpermute_b32 v107, v248, v21
	ds_bpermute_b32 v108, v248, v22
	ds_bpermute_b32 v109, v248, v23
	s_nop 1
	v_pk_mul_f32 v[182:183], v[182:183], s[74:75] op_sel_hi:[1,0]
	v_pk_mul_f32 v[180:181], v[184:185], s[74:75] op_sel_hi:[1,0]
	v_max3_f32 v49, v49, v182, v183
	v_max3_f32 v49, v49, v180, v181
	s_waitcnt lgkmcnt(12)
	v_mfma_f32_16x16x32_bf16 v[184:187], v[110:113], v[134:137], 0
	s_waitcnt lgkmcnt(8)
	v_mfma_f32_16x16x32_bf16 v[184:187], v[114:117], v[44:47], v[184:187]
	s_waitcnt vmcnt(9)
	ds_bpermute_b32 v110, v248, v24
	ds_bpermute_b32 v111, v248, v25
	ds_bpermute_b32 v112, v248, v26
	ds_bpermute_b32 v113, v248, v27
	s_waitcnt vmcnt(8)
	ds_bpermute_b32 v114, v248, v28
	ds_bpermute_b32 v115, v248, v29
	ds_bpermute_b32 v116, v248, v30
	ds_bpermute_b32 v117, v248, v31
	s_nop 1
	v_pk_mul_f32 v[184:185], v[184:185], s[74:75] op_sel_hi:[1,0]
	v_pk_mul_f32 v[178:179], v[186:187], s[74:75] op_sel_hi:[1,0]
	v_max3_f32 v49, v49, v184, v185
	v_max3_f32 v49, v49, v178, v179
	s_waitcnt lgkmcnt(12)
	v_mfma_f32_16x16x32_bf16 v[188:191], v[102:105], v[134:137], 0
	s_waitcnt lgkmcnt(8)
	v_mfma_f32_16x16x32_bf16 v[190:193], v[106:109], v[44:47], v[188:191]
	s_waitcnt vmcnt(7)
	ds_bpermute_b32 v102, v248, v32
	ds_bpermute_b32 v103, v248, v33
	ds_bpermute_b32 v104, v248, v34
	ds_bpermute_b32 v105, v248, v35
	s_waitcnt vmcnt(6)
	ds_bpermute_b32 v106, v248, v36
	ds_bpermute_b32 v107, v248, v37
	ds_bpermute_b32 v108, v248, v38
	ds_bpermute_b32 v109, v248, v39
	s_nop 1
	v_pk_mul_f32 v[190:191], v[190:191], s[74:75] op_sel_hi:[1,0]
	v_pk_mul_f32 v[188:189], v[192:193], s[74:75] op_sel_hi:[1,0]
	v_max3_f32 v49, v49, v190, v191
	v_max3_f32 v49, v49, v188, v189
	s_waitcnt lgkmcnt(12)
	v_mfma_f32_16x16x32_bf16 v[192:195], v[110:113], v[134:137], 0
	s_waitcnt lgkmcnt(8)
	v_mfma_f32_16x16x32_bf16 v[192:195], v[114:117], v[44:47], v[192:195]
	s_waitcnt vmcnt(5)
	ds_bpermute_b32 v110, v248, v40
	ds_bpermute_b32 v111, v248, v41
	ds_bpermute_b32 v112, v248, v42
	ds_bpermute_b32 v113, v248, v43
	s_waitcnt vmcnt(4)
	ds_bpermute_b32 v114, v248, v50
	ds_bpermute_b32 v115, v248, v51
	ds_bpermute_b32 v116, v248, v52
	ds_bpermute_b32 v117, v248, v53
	s_nop 1
	v_pk_mul_f32 v[192:193], v[192:193], s[74:75] op_sel_hi:[1,0]
	v_pk_mul_f32 v[186:187], v[194:195], s[74:75] op_sel_hi:[1,0]
	v_max3_f32 v49, v49, v192, v193
	v_max3_f32 v49, v49, v186, v187
	s_waitcnt lgkmcnt(12)
	v_mfma_f32_16x16x32_bf16 v[196:199], v[102:105], v[134:137], 0
	s_waitcnt lgkmcnt(8)
	v_mfma_f32_16x16x32_bf16 v[196:199], v[106:109], v[44:47], v[196:199]
	s_waitcnt vmcnt(3)
	ds_bpermute_b32 v102, v248, v54
	ds_bpermute_b32 v103, v248, v55
	ds_bpermute_b32 v104, v248, v56
	ds_bpermute_b32 v105, v248, v57
	s_waitcnt vmcnt(2)
	ds_bpermute_b32 v106, v248, v58
	ds_bpermute_b32 v107, v248, v59
	ds_bpermute_b32 v108, v248, v60
	ds_bpermute_b32 v109, v248, v61
	s_nop 1
	v_pk_mul_f32 v[200:201], v[196:197], s[74:75] op_sel_hi:[1,0]
	v_pk_mul_f32 v[198:199], v[198:199], s[74:75] op_sel_hi:[1,0]
	v_max3_f32 v49, v49, v200, v201
	v_max3_f32 v49, v49, v198, v199
	s_waitcnt lgkmcnt(12)
	v_mfma_f32_16x16x32_bf16 v[194:197], v[110:113], v[134:137], 0
	s_waitcnt lgkmcnt(8)
	v_mfma_f32_16x16x32_bf16 v[194:197], v[114:117], v[44:47], v[194:197]
	s_waitcnt vmcnt(1)
	ds_bpermute_b32 v110, v248, v62
	ds_bpermute_b32 v111, v248, v63
	ds_bpermute_b32 v112, v248, v64
	ds_bpermute_b32 v113, v248, v65
	s_waitcnt vmcnt(0)
	ds_bpermute_b32 v114, v248, v66
	ds_bpermute_b32 v115, v248, v67
	ds_bpermute_b32 v116, v248, v68
	ds_bpermute_b32 v117, v248, v69
	s_nop 1
	v_pk_mul_f32 v[202:203], v[194:195], s[74:75] op_sel_hi:[1,0]
	v_pk_mul_f32 v[194:195], v[196:197], s[74:75] op_sel_hi:[1,0]
	v_max3_f32 v49, v49, v202, v203
	v_max3_f32 v49, v49, v194, v195
	s_waitcnt lgkmcnt(12)
	v_mfma_f32_16x16x32_bf16 v[206:209], v[102:105], v[134:137], 0
	s_waitcnt lgkmcnt(8)
	v_mfma_f32_16x16x32_bf16 v[206:209], v[106:109], v[44:47], v[206:209]
	s_nop 7
	v_pk_mul_f32 v[212:213], v[206:207], s[74:75] op_sel_hi:[1,0]
	v_pk_mul_f32 v[210:211], v[208:209], s[74:75] op_sel_hi:[1,0]
	v_max3_f32 v49, v49, v212, v213
	v_max3_f32 v49, v49, v210, v211
	s_waitcnt lgkmcnt(4)
	v_mfma_f32_16x16x32_bf16 v[134:137], v[110:113], v[134:137], 0
	s_waitcnt lgkmcnt(0)
	v_mfma_f32_16x16x32_bf16 v[44:47], v[114:117], v[44:47], v[134:137]
	s_nop 7
	v_pk_mul_f32 v[44:45], v[44:45], s[74:75] op_sel_hi:[1,0]
	s_nop 0
	v_max3_f32 v49, v49, v44, v45
	v_pk_mul_f32 v[204:205], v[46:47], s[74:75] op_sel_hi:[1,0]
	s_nop 0
	v_max3_f32 v49, v49, v204, v205
	s_and_b64 vcc, exec, s[44:45]
	s_cbranch_vccz .Lmy_dsa_fast_nk_skip
	ds_read_u16 v0, v251
	ds_read_u16 v8, v251 offset:32
	ds_read_u16 v16, v251 offset:64
	ds_read_u16 v24, v251 offset:96
	ds_read_u16 v32, v251 offset:128
	ds_read_u16 v40, v251 offset:160
	ds_read_u16 v54, v251 offset:192
	ds_read_u16 v62, v251 offset:224
	s_waitcnt lgkmcnt(0)
	v_lshl_or_b32 v4, v0, 8, v246
	global_load_dwordx4 v[0:3], v4, s[50:51]
	global_load_dwordx4 v[4:7], v4, s[50:51] offset:64
	v_lshl_or_b32 v12, v8, 8, v246
	global_load_dwordx4 v[8:11], v12, s[50:51]
	global_load_dwordx4 v[12:15], v12, s[50:51] offset:64
	v_lshl_or_b32 v20, v16, 8, v246
	global_load_dwordx4 v[16:19], v20, s[50:51]
	global_load_dwordx4 v[20:23], v20, s[50:51] offset:64
	v_lshl_or_b32 v28, v24, 8, v246
	global_load_dwordx4 v[24:27], v28, s[50:51]
	global_load_dwordx4 v[28:31], v28, s[50:51] offset:64
	v_lshl_or_b32 v36, v32, 8, v246
	global_load_dwordx4 v[32:35], v36, s[50:51]
	global_load_dwordx4 v[36:39], v36, s[50:51] offset:64
	v_lshl_or_b32 v50, v40, 8, v246
	global_load_dwordx4 v[40:43], v50, s[50:51]
	global_load_dwordx4 v[50:53], v50, s[50:51] offset:64
	v_lshl_or_b32 v58, v54, 8, v246
	global_load_dwordx4 v[54:57], v58, s[50:51]
	global_load_dwordx4 v[58:61], v58, s[50:51] offset:64
	v_lshl_or_b32 v66, v62, 8, v246
	global_load_dwordx4 v[62:65], v66, s[50:51]
	global_load_dwordx4 v[66:69], v66, s[50:51] offset:64
